# plus cache-warming prefetch loads ahead of the chunk-C q/k and GLA operand staging loops
# speedup vs baseline: 1.0018x; 1.0005x over previous
.LBB0_952:
	s_xor_b64 s[6:7], s[90:91], -1
	s_andn2_b64 vcc, exec, s[6:7]
	s_mov_b64 s[30:31], -1
	s_waitcnt lgkmcnt(0)
	s_barrier
	s_cbranch_vccnz .LBB0_957
	s_mov_b64 s[30:31], exec
	v_readlane_b32 s36, v254, 54
	v_readlane_b32 s37, v254, 55
	s_and_b64 s[36:37], s[30:31], s[36:37]
	s_movk_i32 s62, 0x1ff
	s_mov_b64 exec, s[36:37]
	s_cbranch_execz .LBB0_956
	s_lshl_b32 s4, s21, 7
	s_lshl_b64 s[36:37], s[4:5], 2
	v_readlane_b32 s40, v254, 46
	s_add_u32 s36, s40, s36
	v_readlane_b32 s40, v254, 47
	s_addc_u32 s37, s40, s37
	s_mov_b64 s[40:41], 0
	s_lshl_b32 s4, s4, 1
	v_mov_b32_e32 v0, v122
	v_mov_b32_e32 v1, v59
	v_ashrrev_i32_e32 v212, 4, v1
	v_add_u32_e32 v212, s74, v212
	v_add_u32_e32 v212, 32, v212
	v_mov_b64_e32 v[208:209], s[12:13]
	v_mad_i64_i32 v[208:209], s[60:61], v212, s83, v[208:209]
	v_and_b32_e32 v214, 0x78, v0
	v_ashrrev_i32_e32 v213, 31, v212
	v_lshlrev_b32_e32 v210, 1, v214
	v_mov_b32_e32 v211, 0
	v_lshl_add_u64 v[208:209], v[208:209], 0, s[4:5]
	v_lshl_add_u64 v[208:209], v[208:209], 0, v[210:211]
	v_lshlrev_b64 v[212:213], 11, v[212:213]
	v_add_co_u32_e32 v208, vcc, 0x1000, v208
	v_lshl_add_u64 v[212:213], s[36:37], 0, v[212:213]
	v_lshlrev_b32_e32 v210, 2, v214
	v_addc_co_u32_e32 v209, vcc, 0, v209, vcc
	v_lshl_add_u64 v[212:213], v[212:213], 0, v[210:211]
	global_load_dwordx4 v[204:207], v[208:209], off offset:2048
	global_load_dwordx4 v[204:207], v[208:209], off offset:3072
	global_load_dwordx4 v[204:207], v[212:213], off offset:16
	global_load_dwordx4 v[204:207], v[212:213], off

.LBB0_957:
	s_andn2_b64 vcc, exec, s[30:31]
	s_cbranch_vccnz .LBB0_966
	s_and_saveexec_b64 s[30:31], s[38:39]
	s_cbranch_execz .LBB0_963
	s_lshl_b32 s4, s75, 7
	s_mov_b64 s[36:37], 0
	s_lshl_b32 s4, s4, 1
	v_mov_b32_e32 v4, v122
	v_mov_b32_e32 v5, v59
	v_bfe_u32 v212, v5, 4, 6
	v_or_b32_e32 v208, s74, v212
	v_ashrrev_i32_e32 v209, 31, v208
	v_ashrrev_i32_e32 v210, 1, v5
	v_lshlrev_b64 v[208:209], 11, v[208:209]
	v_and_b32_e32 v210, 0xfffffe00, v210
	v_lshl_add_u64 v[208:209], s[94:95], 0, v[208:209]
	v_ashrrev_i32_e32 v211, 31, v210
	v_lshl_add_u64 v[208:209], v[210:211], 1, v[208:209]
	v_and_b32_e32 v210, 0x78, v4
	v_lshl_add_u64 v[208:209], v[208:209], 0, s[4:5]
	v_lshlrev_b32_e32 v210, 1, v210
	v_mov_b32_e32 v211, 0
	v_lshl_add_u64 v[208:209], v[208:209], 0, v[210:211]
	global_load_dwordx4 v[204:207], v[208:209], off offset:1024
	v_add_co_u32_e32 v210, vcc, 0x10000, v208
	s_nop 1
	v_addc_co_u32_e32 v211, vcc, 0, v209, vcc
	global_load_dwordx4 v[204:207], v[210:211], off
	global_load_dwordx4 v[204:207], v[210:211], off offset:1024
	s_branch .LBB0_961
